# combo13 minus the 20 back-to-back s_setprio 0 / s_setprio 1 toggles inside the MFMA phases (priority stays raised across the 16 MFMAs)
# baseline (speedup 1.0000x reference)
.LBB0_200:
	s_add_u32 s72, s42, 0xfff80000
	s_addc_u32 s73, s43, -1
	s_mov_b32 m0, s57
	s_nop 0
	global_load_lds_dwordx4 v160, s[72:73]
	s_mov_b32 m0, s58
	s_nop 0
	global_load_lds_dwordx4 v164, s[72:73]
	ds_read_b128 v[16:19], v186
	ds_read_b128 v[20:23], v187
	ds_read_b128 v[24:27], v188
	ds_read_b128 v[28:31], v189
	ds_read_b128 v[0:3], v190
	ds_read_b128 v[4:7], v191
	ds_read_b128 v[8:11], v192
	ds_read_b128 v[12:15], v193
	s_add_u32 s44, s42, 0xfff80080
	s_addc_u32 s45, s43, -1
	s_cmp_eq_u32 s68, 28
	s_cselect_b32 s47, s31, s45
	s_cselect_b32 s46, s35, s44
	s_cselect_b32 s45, s29, s67
	s_cselect_b32 s44, s39, s66
	s_add_i32 m0, s27, 0xc000
	ds_read_b128 v[178:181], v218
	ds_read_b128 v[182:185], v218 offset:1024
	ds_read_b128 v[222:225], v218 offset:2048
	ds_read_b128 v[226:229], v218 offset:3072
	ds_read_b128 v[230:233], v218 offset:4096
	ds_read_b128 v[234:237], v218 offset:5120
	ds_read_b128 v[238:241], v218 offset:6144
	ds_read_b128 v[242:245], v218 offset:7168
	global_load_lds_dwordx4 v172, s[42:43]
	s_add_i32 m0, s27, 0xe000
	s_nop 0
	global_load_lds_dwordx4 v174, s[42:43]
	s_waitcnt vmcnt(8)
	s_waitcnt lgkmcnt(0)
	s_barrier
	s_setprio 1
	s_waitcnt lgkmcnt(0)
	v_mfma_f32_16x16x128_f8f6f4 v[156:159], v[16:23], v[178:185], v[156:159]
	v_mfma_f32_16x16x128_f8f6f4 v[152:155], v[24:31], v[178:185], v[152:155]
	v_mfma_f32_16x16x128_f8f6f4 v[144:147], v[24:31], v[222:229], v[144:147]
	v_mfma_f32_16x16x128_f8f6f4 v[148:151], v[16:23], v[222:229], v[148:151]
	v_mfma_f32_16x16x128_f8f6f4 v[140:143], v[16:23], v[230:237], v[140:143]
	v_mfma_f32_16x16x128_f8f6f4 v[136:139], v[24:31], v[230:237], v[136:139]
	v_mfma_f32_16x16x128_f8f6f4 v[128:131], v[24:31], v[238:245], v[128:131]
	v_mfma_f32_16x16x128_f8f6f4 v[132:135], v[16:23], v[238:245], v[132:135]
	v_mfma_f32_16x16x128_f8f6f4 v[100:103], v[0:7], v[238:245], v[100:103]
	v_mfma_f32_16x16x128_f8f6f4 v[96:99], v[8:15], v[238:245], v[96:99]
	v_mfma_f32_16x16x128_f8f6f4 v[104:107], v[8:15], v[230:237], v[104:107]
	v_mfma_f32_16x16x128_f8f6f4 v[108:111], v[0:7], v[230:237], v[108:111]
	v_mfma_f32_16x16x128_f8f6f4 v[116:119], v[0:7], v[222:229], v[116:119]
	v_mfma_f32_16x16x128_f8f6f4 v[112:115], v[8:15], v[222:229], v[112:115]
	v_mfma_f32_16x16x128_f8f6f4 v[120:123], v[8:15], v[178:185], v[120:123]
	v_mfma_f32_16x16x128_f8f6f4 v[124:127], v[0:7], v[178:185], v[124:127]
	s_setprio 0
	s_barrier
	s_mov_b32 m0, s33
	v_lshl_add_u64 v[178:179], s[44:45], 0, v[162:163]
	s_add_u32 s70, s44, 0x80000
	ds_read_b128 v[222:225], v218 offset:16384
	ds_read_b128 v[226:229], v218 offset:17408
	ds_read_b128 v[230:233], v218 offset:18432
	ds_read_b128 v[234:237], v218 offset:19456
	ds_read_b128 v[238:241], v218 offset:20480
	ds_read_b128 v[242:245], v218 offset:21504
	ds_read_b128 v[246:249], v218 offset:22528
	ds_read_b128 v[250:253], v218 offset:23552
	global_load_lds_dwordx4 v[178:179], off
	v_lshl_add_u64 v[180:181], s[44:45], 0, v[166:167]
	s_mov_b32 m0, s48
	s_addc_u32 s71, s45, 0
	global_load_lds_dwordx4 v[180:181], off
	s_mov_b32 m0, s49
	s_nop 0
	global_load_lds_dwordx4 v162, s[70:71]
	s_mov_b32 m0, s50
	s_nop 0
	global_load_lds_dwordx4 v166, s[70:71]
	s_waitcnt vmcnt(6)
	s_waitcnt lgkmcnt(0)
	s_barrier
	s_setprio 1
	s_waitcnt lgkmcnt(0)
	v_mfma_f32_16x16x128_f8f6f4 v[92:95], v[16:23], v[222:229], v[92:95]
	v_mfma_f32_16x16x128_f8f6f4 v[88:91], v[24:31], v[222:229], v[88:91]
	v_mfma_f32_16x16x128_f8f6f4 v[80:83], v[24:31], v[230:237], v[80:83]
	v_mfma_f32_16x16x128_f8f6f4 v[84:87], v[16:23], v[230:237], v[84:87]
	v_mfma_f32_16x16x128_f8f6f4 v[76:79], v[16:23], v[238:245], v[76:79]
	v_mfma_f32_16x16x128_f8f6f4 v[72:75], v[24:31], v[238:245], v[72:75]
	v_mfma_f32_16x16x128_f8f6f4 v[64:67], v[24:31], v[246:253], v[64:67]
	v_mfma_f32_16x16x128_f8f6f4 v[68:71], v[16:23], v[246:253], v[68:71]
	v_mfma_f32_16x16x128_f8f6f4 v[36:39], v[0:7], v[246:253], v[36:39]
	v_mfma_f32_16x16x128_f8f6f4 v[32:35], v[8:15], v[246:253], v[32:35]
	v_mfma_f32_16x16x128_f8f6f4 v[40:43], v[8:15], v[238:245], v[40:43]
	v_mfma_f32_16x16x128_f8f6f4 v[44:47], v[0:7], v[238:245], v[44:47]
	v_mfma_f32_16x16x128_f8f6f4 v[52:55], v[0:7], v[230:237], v[52:55]
	v_mfma_f32_16x16x128_f8f6f4 v[48:51], v[8:15], v[230:237], v[48:51]
	v_mfma_f32_16x16x128_f8f6f4 v[56:59], v[8:15], v[222:229], v[56:59]
	v_mfma_f32_16x16x128_f8f6f4 v[60:63], v[0:7], v[222:229], v[60:63]
	s_setprio 0
	s_barrier
	s_mov_b32 m0, s27
	s_nop 0
	global_load_lds_dwordx4 v160, s[46:47]
	s_mov_b32 m0, s51
	s_nop 0
	global_load_lds_dwordx4 v164, s[46:47]
	ds_read_b128 v[0:3], v194
	ds_read_b128 v[4:7], v195
	ds_read_b128 v[8:11], v196
	ds_read_b128 v[12:15], v197
	ds_read_b128 v[16:19], v198
	ds_read_b128 v[20:23], v199
	ds_read_b128 v[24:27], v200
	ds_read_b128 v[28:31], v201
	s_add_u32 s46, s46, 0x80000
	s_addc_u32 s47, s47, 0
	s_mov_b32 m0, s52
	ds_read_b128 v[222:225], v218 offset:32768
	ds_read_b128 v[226:229], v218 offset:33792
	ds_read_b128 v[230:233], v218 offset:34816
	ds_read_b128 v[234:237], v218 offset:35840
	ds_read_b128 v[238:241], v218 offset:36864
	ds_read_b128 v[242:245], v218 offset:37888
	ds_read_b128 v[246:249], v218 offset:38912
	ds_read_b128 v[250:253], v218 offset:39936
	global_load_lds_dwordx4 v160, s[46:47]
	s_mov_b32 m0, s53
	s_nop 0
	global_load_lds_dwordx4 v164, s[46:47]
	s_waitcnt vmcnt(8)
	s_waitcnt lgkmcnt(0)
	s_barrier
	s_setprio 1
	s_waitcnt lgkmcnt(0)
	v_mfma_f32_16x16x128_f8f6f4 v[156:159], v[0:7], v[222:229], v[156:159]
	v_mfma_f32_16x16x128_f8f6f4 v[152:155], v[8:15], v[222:229], v[152:155]
	v_mfma_f32_16x16x128_f8f6f4 v[144:147], v[8:15], v[230:237], v[144:147]
	v_mfma_f32_16x16x128_f8f6f4 v[148:151], v[0:7], v[230:237], v[148:151]
	v_mfma_f32_16x16x128_f8f6f4 v[140:143], v[0:7], v[238:245], v[140:143]
	v_mfma_f32_16x16x128_f8f6f4 v[136:139], v[8:15], v[238:245], v[136:139]
	v_mfma_f32_16x16x128_f8f6f4 v[128:131], v[8:15], v[246:253], v[128:131]
	v_mfma_f32_16x16x128_f8f6f4 v[132:135], v[0:7], v[246:253], v[132:135]
	v_mfma_f32_16x16x128_f8f6f4 v[100:103], v[16:23], v[246:253], v[100:103]
	v_mfma_f32_16x16x128_f8f6f4 v[96:99], v[24:31], v[246:253], v[96:99]
	v_mfma_f32_16x16x128_f8f6f4 v[104:107], v[24:31], v[238:245], v[104:107]
	v_mfma_f32_16x16x128_f8f6f4 v[108:111], v[16:23], v[238:245], v[108:111]
	v_mfma_f32_16x16x128_f8f6f4 v[116:119], v[16:23], v[230:237], v[116:119]
	v_mfma_f32_16x16x128_f8f6f4 v[112:115], v[24:31], v[230:237], v[112:115]
	v_mfma_f32_16x16x128_f8f6f4 v[120:123], v[24:31], v[222:229], v[120:123]
	v_mfma_f32_16x16x128_f8f6f4 v[124:127], v[16:23], v[222:229], v[124:127]
	s_setprio 0
	s_barrier
	s_mov_b32 m0, s55
	v_lshl_add_u64 v[176:177], v[178:179], 0, s[20:21]
	s_add_u32 s44, s44, 0x80080
	ds_read_b128 v[222:225], v218 offset:49152
	ds_read_b128 v[226:229], v218 offset:50176
	ds_read_b128 v[230:233], v218 offset:51200
	ds_read_b128 v[234:237], v218 offset:52224
	ds_read_b128 v[238:241], v218 offset:53248
	ds_read_b128 v[242:245], v218 offset:54272
	ds_read_b128 v[246:249], v218 offset:55296
	ds_read_b128 v[250:253], v218 offset:56320
	global_load_lds_dwordx4 v[176:177], off
	v_lshl_add_u64 v[176:177], v[180:181], 0, s[20:21]
	s_mov_b32 m0, s56
	s_addc_u32 s45, s45, 0
	global_load_lds_dwordx4 v[176:177], off
	s_mov_b32 m0, s59
	s_nop 0
	global_load_lds_dwordx4 v162, s[44:45]
	s_mov_b32 m0, s60
	s_nop 0
	global_load_lds_dwordx4 v166, s[44:45]
	s_waitcnt vmcnt(6)
	s_waitcnt lgkmcnt(0)
	s_barrier
	s_setprio 1
	s_waitcnt lgkmcnt(0)
	v_mfma_f32_16x16x128_f8f6f4 v[92:95], v[0:7], v[222:229], v[92:95]
	v_mfma_f32_16x16x128_f8f6f4 v[88:91], v[8:15], v[222:229], v[88:91]
	v_mfma_f32_16x16x128_f8f6f4 v[80:83], v[8:15], v[230:237], v[80:83]
	v_mfma_f32_16x16x128_f8f6f4 v[84:87], v[0:7], v[230:237], v[84:87]
	v_mfma_f32_16x16x128_f8f6f4 v[76:79], v[0:7], v[238:245], v[76:79]
	v_mfma_f32_16x16x128_f8f6f4 v[72:75], v[8:15], v[238:245], v[72:75]
	v_mfma_f32_16x16x128_f8f6f4 v[64:67], v[8:15], v[246:253], v[64:67]
	v_mfma_f32_16x16x128_f8f6f4 v[68:71], v[0:7], v[246:253], v[68:71]
	v_mfma_f32_16x16x128_f8f6f4 v[36:39], v[16:23], v[246:253], v[36:39]
	v_mfma_f32_16x16x128_f8f6f4 v[32:35], v[24:31], v[246:253], v[32:35]
	v_mfma_f32_16x16x128_f8f6f4 v[40:43], v[24:31], v[238:245], v[40:43]
	v_mfma_f32_16x16x128_f8f6f4 v[44:47], v[16:23], v[238:245], v[44:47]
	v_mfma_f32_16x16x128_f8f6f4 v[52:55], v[16:23], v[230:237], v[52:55]
	v_mfma_f32_16x16x128_f8f6f4 v[48:51], v[24:31], v[230:237], v[48:51]
	v_mfma_f32_16x16x128_f8f6f4 v[56:59], v[24:31], v[222:229], v[56:59]
	v_mfma_f32_16x16x128_f8f6f4 v[60:63], v[16:23], v[222:229], v[60:63]
	s_setprio 0
	s_barrier
	s_add_i32 s68, s68, 2
	s_add_u32 s42, s42, 0x100
	s_addc_u32 s43, s43, 0
	s_add_u32 s66, s66, 0x100
	s_addc_u32 s67, s67, 0
	s_cmp_gt_u32 s68, 29
	s_cbranch_scc0 .LBB0_200
	s_nop 15
	s_nop 15
	s_and_b64 vcc, exec, s[22:23]
	s_cbranch_vccz .LBB0_203
	s_barrier

.LBB0_562:
	s_add_u32 s72, s30, 0xfff80000
	s_addc_u32 s73, s31, -1
	s_mov_b32 m0, s49
	s_nop 0
	global_load_lds_dwordx4 v160, s[72:73]
	s_mov_b32 m0, s50
	s_nop 0
	global_load_lds_dwordx4 v162, s[72:73]
	ds_read_b128 v[16:19], v181
	ds_read_b128 v[20:23], v182
	ds_read_b128 v[24:27], v183
	ds_read_b128 v[28:31], v184
	ds_read_b128 v[0:3], v185
	ds_read_b128 v[4:7], v186
	ds_read_b128 v[8:11], v187
	ds_read_b128 v[12:15], v188
	s_add_u32 s34, s30, 0xfff80080
	s_addc_u32 s35, s31, -1
	s_cmp_eq_u32 s59, 28
	s_cselect_b32 s37, s23, s35
	s_cselect_b32 s36, s55, s34
	s_cselect_b32 s35, s21, s58
	s_cselect_b32 s34, s56, s57
	s_add_i32 m0, s29, 0xc000
	ds_read_b128 v[172:175], v198
	ds_read_b128 v[176:179], v198 offset:1024
	ds_read_b128 v[200:203], v198 offset:2048
	ds_read_b128 v[204:207], v198 offset:3072
	ds_read_b128 v[208:211], v198 offset:4096
	ds_read_b128 v[212:215], v198 offset:5120
	ds_read_b128 v[216:219], v198 offset:6144
	ds_read_b128 v[220:223], v198 offset:7168
	global_load_lds_dwordx4 v164, s[30:31]
	s_add_i32 m0, s29, 0xe000
	s_nop 0
	global_load_lds_dwordx4 v166, s[30:31]
	s_waitcnt vmcnt(8)
	s_waitcnt lgkmcnt(0)
	s_barrier
	s_setprio 1
	s_waitcnt lgkmcnt(0)
	v_mfma_f32_16x16x128_f8f6f4 v[156:159], v[16:23], v[172:179], v[156:159]
	v_mfma_f32_16x16x128_f8f6f4 v[152:155], v[24:31], v[172:179], v[152:155]
	v_mfma_f32_16x16x128_f8f6f4 v[144:147], v[24:31], v[200:207], v[144:147]
	v_mfma_f32_16x16x128_f8f6f4 v[148:151], v[16:23], v[200:207], v[148:151]
	v_mfma_f32_16x16x128_f8f6f4 v[124:127], v[16:23], v[208:215], v[124:127]
	v_mfma_f32_16x16x128_f8f6f4 v[120:123], v[24:31], v[208:215], v[120:123]
	v_mfma_f32_16x16x128_f8f6f4 v[112:115], v[24:31], v[216:223], v[112:115]
	v_mfma_f32_16x16x128_f8f6f4 v[116:119], v[16:23], v[216:223], v[116:119]
	v_mfma_f32_16x16x128_f8f6f4 v[100:103], v[0:7], v[216:223], v[100:103]
	v_mfma_f32_16x16x128_f8f6f4 v[96:99], v[8:15], v[216:223], v[96:99]
	v_mfma_f32_16x16x128_f8f6f4 v[104:107], v[8:15], v[208:215], v[104:107]
	v_mfma_f32_16x16x128_f8f6f4 v[108:111], v[0:7], v[208:215], v[108:111]
	v_mfma_f32_16x16x128_f8f6f4 v[132:135], v[0:7], v[200:207], v[132:135]
	v_mfma_f32_16x16x128_f8f6f4 v[128:131], v[8:15], v[200:207], v[128:131]
	v_mfma_f32_16x16x128_f8f6f4 v[136:139], v[8:15], v[172:179], v[136:139]
	v_mfma_f32_16x16x128_f8f6f4 v[140:143], v[0:7], v[172:179], v[140:143]
	s_setprio 0
	s_barrier
	s_mov_b32 m0, s33
	v_lshl_add_u64 v[172:173], s[34:35], 0, v[160:161]
	s_add_u32 s60, s34, 0x80000
	ds_read_b128 v[200:203], v198 offset:16384
	ds_read_b128 v[204:207], v198 offset:17408
	ds_read_b128 v[208:211], v198 offset:18432
	ds_read_b128 v[212:215], v198 offset:19456
	ds_read_b128 v[216:219], v198 offset:20480
	ds_read_b128 v[220:223], v198 offset:21504
	ds_read_b128 v[224:227], v198 offset:22528
	ds_read_b128 v[228:231], v198 offset:23552
	global_load_lds_dwordx4 v[172:173], off
	v_lshl_add_u64 v[174:175], s[34:35], 0, v[162:163]
	s_mov_b32 m0, s38
	s_addc_u32 s61, s35, 0
	global_load_lds_dwordx4 v[174:175], off
	s_mov_b32 m0, s39
	s_nop 0
	global_load_lds_dwordx4 v160, s[60:61]
	s_mov_b32 m0, s40
	s_nop 0
	global_load_lds_dwordx4 v162, s[60:61]
	s_waitcnt vmcnt(6)
	s_waitcnt lgkmcnt(0)
	s_barrier
	s_setprio 1
	s_waitcnt lgkmcnt(0)
	v_mfma_f32_16x16x128_f8f6f4 v[92:95], v[16:23], v[200:207], v[92:95]
	v_mfma_f32_16x16x128_f8f6f4 v[88:91], v[24:31], v[200:207], v[88:91]
	v_mfma_f32_16x16x128_f8f6f4 v[80:83], v[24:31], v[208:215], v[80:83]
	v_mfma_f32_16x16x128_f8f6f4 v[84:87], v[16:23], v[208:215], v[84:87]
	v_mfma_f32_16x16x128_f8f6f4 v[60:63], v[16:23], v[216:223], v[60:63]
	v_mfma_f32_16x16x128_f8f6f4 v[56:59], v[24:31], v[216:223], v[56:59]
	v_mfma_f32_16x16x128_f8f6f4 v[48:51], v[24:31], v[224:231], v[48:51]
	v_mfma_f32_16x16x128_f8f6f4 v[52:55], v[16:23], v[224:231], v[52:55]
	v_mfma_f32_16x16x128_f8f6f4 v[36:39], v[0:7], v[224:231], v[36:39]
	v_mfma_f32_16x16x128_f8f6f4 v[32:35], v[8:15], v[224:231], v[32:35]
	v_mfma_f32_16x16x128_f8f6f4 v[40:43], v[8:15], v[216:223], v[40:43]
	v_mfma_f32_16x16x128_f8f6f4 v[44:47], v[0:7], v[216:223], v[44:47]
	v_mfma_f32_16x16x128_f8f6f4 v[68:71], v[0:7], v[208:215], v[68:71]
	v_mfma_f32_16x16x128_f8f6f4 v[64:67], v[8:15], v[208:215], v[64:67]
	v_mfma_f32_16x16x128_f8f6f4 v[72:75], v[8:15], v[200:207], v[72:75]
	v_mfma_f32_16x16x128_f8f6f4 v[76:79], v[0:7], v[200:207], v[76:79]
	s_setprio 0
	s_barrier
	s_mov_b32 m0, s29
	s_nop 0
	global_load_lds_dwordx4 v160, s[36:37]
	s_mov_b32 m0, s41
	s_nop 0
	global_load_lds_dwordx4 v162, s[36:37]
	ds_read_b128 v[0:3], v189
	ds_read_b128 v[4:7], v190
	ds_read_b128 v[8:11], v191
	ds_read_b128 v[12:15], v192
	ds_read_b128 v[16:19], v193
	ds_read_b128 v[20:23], v194
	ds_read_b128 v[24:27], v195
	ds_read_b128 v[28:31], v196
	s_add_u32 s36, s36, 0x80000
	s_addc_u32 s37, s37, 0
	s_mov_b32 m0, s42
	ds_read_b128 v[200:203], v198 offset:32768
	ds_read_b128 v[204:207], v198 offset:33792
	ds_read_b128 v[208:211], v198 offset:34816
	ds_read_b128 v[212:215], v198 offset:35840
	ds_read_b128 v[216:219], v198 offset:36864
	ds_read_b128 v[220:223], v198 offset:37888
	ds_read_b128 v[224:227], v198 offset:38912
	ds_read_b128 v[228:231], v198 offset:39936
	global_load_lds_dwordx4 v160, s[36:37]
	s_mov_b32 m0, s43
	s_nop 0
	global_load_lds_dwordx4 v162, s[36:37]
	s_waitcnt vmcnt(8)
	s_waitcnt lgkmcnt(0)
	s_barrier
	s_setprio 1
	s_waitcnt lgkmcnt(0)
	v_mfma_f32_16x16x128_f8f6f4 v[156:159], v[0:7], v[200:207], v[156:159]
	v_mfma_f32_16x16x128_f8f6f4 v[152:155], v[8:15], v[200:207], v[152:155]
	v_mfma_f32_16x16x128_f8f6f4 v[144:147], v[8:15], v[208:215], v[144:147]
	v_mfma_f32_16x16x128_f8f6f4 v[148:151], v[0:7], v[208:215], v[148:151]
	v_mfma_f32_16x16x128_f8f6f4 v[124:127], v[0:7], v[216:223], v[124:127]
	v_mfma_f32_16x16x128_f8f6f4 v[120:123], v[8:15], v[216:223], v[120:123]
	v_mfma_f32_16x16x128_f8f6f4 v[112:115], v[8:15], v[224:231], v[112:115]
	v_mfma_f32_16x16x128_f8f6f4 v[116:119], v[0:7], v[224:231], v[116:119]
	v_mfma_f32_16x16x128_f8f6f4 v[100:103], v[16:23], v[224:231], v[100:103]
	v_mfma_f32_16x16x128_f8f6f4 v[96:99], v[24:31], v[224:231], v[96:99]
	v_mfma_f32_16x16x128_f8f6f4 v[104:107], v[24:31], v[216:223], v[104:107]
	v_mfma_f32_16x16x128_f8f6f4 v[108:111], v[16:23], v[216:223], v[108:111]
	v_mfma_f32_16x16x128_f8f6f4 v[132:135], v[16:23], v[208:215], v[132:135]
	v_mfma_f32_16x16x128_f8f6f4 v[128:131], v[24:31], v[208:215], v[128:131]
	v_mfma_f32_16x16x128_f8f6f4 v[136:139], v[24:31], v[200:207], v[136:139]
	v_mfma_f32_16x16x128_f8f6f4 v[140:143], v[16:23], v[200:207], v[140:143]
	s_setprio 0
	s_barrier
	s_mov_b32 m0, s47
	v_lshl_add_u64 v[172:173], v[172:173], 0, s[14:15]
	s_add_u32 s34, s34, 0x80080
	ds_read_b128 v[200:203], v198 offset:49152
	ds_read_b128 v[204:207], v198 offset:50176
	ds_read_b128 v[208:211], v198 offset:51200
	ds_read_b128 v[212:215], v198 offset:52224
	ds_read_b128 v[216:219], v198 offset:53248
	ds_read_b128 v[220:223], v198 offset:54272
	ds_read_b128 v[224:227], v198 offset:55296
	ds_read_b128 v[228:231], v198 offset:56320
	global_load_lds_dwordx4 v[172:173], off
	v_lshl_add_u64 v[172:173], v[174:175], 0, s[14:15]
	s_mov_b32 m0, s48
	s_addc_u32 s35, s35, 0
	global_load_lds_dwordx4 v[172:173], off
	s_mov_b32 m0, s51
	s_nop 0
	global_load_lds_dwordx4 v160, s[34:35]
	s_mov_b32 m0, s52
	s_nop 0
	global_load_lds_dwordx4 v162, s[34:35]
	s_waitcnt vmcnt(6)
	s_waitcnt lgkmcnt(0)
	s_barrier
	s_setprio 1
	s_waitcnt lgkmcnt(0)
	v_mfma_f32_16x16x128_f8f6f4 v[92:95], v[0:7], v[200:207], v[92:95]
	v_mfma_f32_16x16x128_f8f6f4 v[88:91], v[8:15], v[200:207], v[88:91]
	v_mfma_f32_16x16x128_f8f6f4 v[80:83], v[8:15], v[208:215], v[80:83]
	v_mfma_f32_16x16x128_f8f6f4 v[84:87], v[0:7], v[208:215], v[84:87]
	v_mfma_f32_16x16x128_f8f6f4 v[60:63], v[0:7], v[216:223], v[60:63]
	v_mfma_f32_16x16x128_f8f6f4 v[56:59], v[8:15], v[216:223], v[56:59]
	v_mfma_f32_16x16x128_f8f6f4 v[48:51], v[8:15], v[224:231], v[48:51]
	v_mfma_f32_16x16x128_f8f6f4 v[52:55], v[0:7], v[224:231], v[52:55]
	v_mfma_f32_16x16x128_f8f6f4 v[36:39], v[16:23], v[224:231], v[36:39]
	v_mfma_f32_16x16x128_f8f6f4 v[32:35], v[24:31], v[224:231], v[32:35]
	v_mfma_f32_16x16x128_f8f6f4 v[40:43], v[24:31], v[216:223], v[40:43]
	v_mfma_f32_16x16x128_f8f6f4 v[44:47], v[16:23], v[216:223], v[44:47]
	v_mfma_f32_16x16x128_f8f6f4 v[68:71], v[16:23], v[208:215], v[68:71]
	v_mfma_f32_16x16x128_f8f6f4 v[64:67], v[24:31], v[208:215], v[64:67]
	v_mfma_f32_16x16x128_f8f6f4 v[72:75], v[24:31], v[200:207], v[72:75]
	v_mfma_f32_16x16x128_f8f6f4 v[76:79], v[16:23], v[200:207], v[76:79]
	s_setprio 0
	s_barrier
	s_add_i32 s59, s59, 2
	s_add_u32 s30, s30, 0x100
	s_addc_u32 s31, s31, 0
	s_add_u32 s57, s57, 0x100
	s_addc_u32 s58, s58, 0
	s_cmp_gt_u32 s59, 29
	s_cbranch_scc0 .LBB0_562
	s_nop 15
	s_nop 15
	s_and_b64 vcc, exec, s[16:17]
	s_cbranch_vccz .LBB0_565
	s_barrier

.LBB0_687:
	s_add_u32 s72, s24, 0xfff00000
	s_addc_u32 s73, s25, -1
	s_mov_b32 m0, s44
	s_nop 0
	global_load_lds_dwordx4 v128, s[72:73]
	s_mov_b32 m0, s45
	s_nop 0
	global_load_lds_dwordx4 v130, s[72:73]
	ds_read_b128 v[160:163], v142
	ds_read_b128 v[164:167], v143
	ds_read_b128 v[168:171], v144
	ds_read_b128 v[172:175], v145
	ds_read_b128 v[176:179], v146
	ds_read_b128 v[180:183], v147
	ds_read_b128 v[184:187], v148
	ds_read_b128 v[188:191], v149
	s_add_u32 s26, s24, 0xfff00080
	s_addc_u32 s27, s25, -1
	s_cmp_eq_u32 s54, 60
	s_cselect_b32 s29, s19, s27
	s_cselect_b32 s28, s50, s26
	s_cselect_b32 s27, s17, s53
	s_cselect_b32 s26, s51, s52
	s_add_i32 m0, s33, 0xc000
	ds_read_b128 v[192:195], v158
	ds_read_b128 v[196:199], v158 offset:1024
	ds_read_b128 v[200:203], v158 offset:2048
	ds_read_b128 v[204:207], v158 offset:3072
	ds_read_b128 v[208:211], v158 offset:4096
	ds_read_b128 v[212:215], v158 offset:5120
	ds_read_b128 v[216:219], v158 offset:6144
	ds_read_b128 v[220:223], v158 offset:7168
	global_load_lds_dwordx4 v134, s[24:25]
	s_add_i32 m0, s33, 0xe000
	s_nop 0
	global_load_lds_dwordx4 v136, s[24:25]
	s_waitcnt vmcnt(8)
	s_waitcnt lgkmcnt(0)
	s_barrier
	s_setprio 1
	s_waitcnt lgkmcnt(0)
	v_mfma_f32_16x16x32_bf16 v[124:127], v[160:163], v[192:195], v[124:127]
	v_mfma_f32_16x16x32_bf16 v[120:123], v[168:171], v[192:195], v[120:123]
	v_mfma_f32_16x16x32_bf16 v[112:115], v[168:171], v[200:203], v[112:115]
	v_mfma_f32_16x16x32_bf16 v[116:119], v[160:163], v[200:203], v[116:119]
	v_mfma_f32_16x16x32_bf16 v[108:111], v[160:163], v[208:211], v[108:111]
	v_mfma_f32_16x16x32_bf16 v[104:107], v[168:171], v[208:211], v[104:107]
	v_mfma_f32_16x16x32_bf16 v[96:99], v[168:171], v[216:219], v[96:99]
	v_mfma_f32_16x16x32_bf16 v[100:103], v[160:163], v[216:219], v[100:103]
	v_mfma_f32_16x16x32_bf16 v[124:127], v[164:167], v[196:199], v[124:127]
	v_mfma_f32_16x16x32_bf16 v[120:123], v[172:175], v[196:199], v[120:123]
	v_mfma_f32_16x16x32_bf16 v[112:115], v[172:175], v[204:207], v[112:115]
	v_mfma_f32_16x16x32_bf16 v[116:119], v[164:167], v[204:207], v[116:119]
	v_mfma_f32_16x16x32_bf16 v[108:111], v[164:167], v[212:215], v[108:111]
	v_mfma_f32_16x16x32_bf16 v[104:107], v[172:175], v[212:215], v[104:107]
	v_mfma_f32_16x16x32_bf16 v[96:99], v[172:175], v[220:223], v[96:99]
	v_mfma_f32_16x16x32_bf16 v[100:103], v[164:167], v[220:223], v[100:103]
	v_mfma_f32_16x16x32_bf16 v[92:95], v[176:179], v[192:195], v[92:95]
	v_mfma_f32_16x16x32_bf16 v[88:91], v[184:187], v[192:195], v[88:91]
	v_mfma_f32_16x16x32_bf16 v[80:83], v[184:187], v[200:203], v[80:83]
	v_mfma_f32_16x16x32_bf16 v[84:87], v[176:179], v[200:203], v[84:87]
	v_mfma_f32_16x16x32_bf16 v[76:79], v[176:179], v[208:211], v[76:79]
	v_mfma_f32_16x16x32_bf16 v[72:75], v[184:187], v[208:211], v[72:75]
	v_mfma_f32_16x16x32_bf16 v[64:67], v[184:187], v[216:219], v[64:67]
	v_mfma_f32_16x16x32_bf16 v[68:71], v[176:179], v[216:219], v[68:71]
	v_mfma_f32_16x16x32_bf16 v[92:95], v[180:183], v[196:199], v[92:95]
	v_mfma_f32_16x16x32_bf16 v[88:91], v[188:191], v[196:199], v[88:91]
	v_mfma_f32_16x16x32_bf16 v[80:83], v[188:191], v[204:207], v[80:83]
	v_mfma_f32_16x16x32_bf16 v[84:87], v[180:183], v[204:207], v[84:87]
	v_mfma_f32_16x16x32_bf16 v[76:79], v[180:183], v[212:215], v[76:79]
	v_mfma_f32_16x16x32_bf16 v[72:75], v[188:191], v[212:215], v[72:75]
	v_mfma_f32_16x16x32_bf16 v[64:67], v[188:191], v[220:223], v[64:67]
	v_mfma_f32_16x16x32_bf16 v[68:71], v[180:183], v[220:223], v[68:71]
	s_setprio 0
	s_barrier
	s_mov_b32 m0, s34
	v_lshl_add_u64 v[224:225], s[26:27], 0, v[128:129]
	s_add_u32 s56, s26, 0x100000
	ds_read_b128 v[192:195], v158 offset:16384
	ds_read_b128 v[196:199], v158 offset:17408
	ds_read_b128 v[200:203], v158 offset:18432
	ds_read_b128 v[204:207], v158 offset:19456
	ds_read_b128 v[208:211], v158 offset:20480
	ds_read_b128 v[212:215], v158 offset:21504
	ds_read_b128 v[216:219], v158 offset:22528
	ds_read_b128 v[220:223], v158 offset:23552
	global_load_lds_dwordx4 v[224:225], off
	v_lshl_add_u64 v[226:227], s[26:27], 0, v[130:131]
	s_mov_b32 m0, s35
	s_addc_u32 s57, s27, 0
	global_load_lds_dwordx4 v[226:227], off
	s_mov_b32 m0, s36
	s_nop 0
	global_load_lds_dwordx4 v128, s[56:57]
	s_mov_b32 m0, s37
	s_nop 0
	global_load_lds_dwordx4 v130, s[56:57]
	s_waitcnt vmcnt(6)
	s_waitcnt lgkmcnt(0)
	s_barrier
	s_setprio 1
	s_waitcnt lgkmcnt(0)
	v_mfma_f32_16x16x32_bf16 v[60:63], v[160:163], v[192:195], v[60:63]
	v_mfma_f32_16x16x32_bf16 v[56:59], v[168:171], v[192:195], v[56:59]
	v_mfma_f32_16x16x32_bf16 v[48:51], v[168:171], v[200:203], v[48:51]
	v_mfma_f32_16x16x32_bf16 v[52:55], v[160:163], v[200:203], v[52:55]
	v_mfma_f32_16x16x32_bf16 v[44:47], v[160:163], v[208:211], v[44:47]
	v_mfma_f32_16x16x32_bf16 v[40:43], v[168:171], v[208:211], v[40:43]
	v_mfma_f32_16x16x32_bf16 v[32:35], v[168:171], v[216:219], v[32:35]
	v_mfma_f32_16x16x32_bf16 v[36:39], v[160:163], v[216:219], v[36:39]
	v_mfma_f32_16x16x32_bf16 v[60:63], v[164:167], v[196:199], v[60:63]
	v_mfma_f32_16x16x32_bf16 v[56:59], v[172:175], v[196:199], v[56:59]
	v_mfma_f32_16x16x32_bf16 v[48:51], v[172:175], v[204:207], v[48:51]
	v_mfma_f32_16x16x32_bf16 v[52:55], v[164:167], v[204:207], v[52:55]
	v_mfma_f32_16x16x32_bf16 v[44:47], v[164:167], v[212:215], v[44:47]
	v_mfma_f32_16x16x32_bf16 v[40:43], v[172:175], v[212:215], v[40:43]
	v_mfma_f32_16x16x32_bf16 v[32:35], v[172:175], v[220:223], v[32:35]
	v_mfma_f32_16x16x32_bf16 v[36:39], v[164:167], v[220:223], v[36:39]
	v_mfma_f32_16x16x32_bf16 v[28:31], v[176:179], v[192:195], v[28:31]
	v_mfma_f32_16x16x32_bf16 v[24:27], v[184:187], v[192:195], v[24:27]
	v_mfma_f32_16x16x32_bf16 v[16:19], v[184:187], v[200:203], v[16:19]
	v_mfma_f32_16x16x32_bf16 v[20:23], v[176:179], v[200:203], v[20:23]
	v_mfma_f32_16x16x32_bf16 v[12:15], v[176:179], v[208:211], v[12:15]
	v_mfma_f32_16x16x32_bf16 v[8:11], v[184:187], v[208:211], v[8:11]
	v_mfma_f32_16x16x32_bf16 v[0:3], v[184:187], v[216:219], v[0:3]
	v_mfma_f32_16x16x32_bf16 v[4:7], v[176:179], v[216:219], v[4:7]
	v_mfma_f32_16x16x32_bf16 v[28:31], v[180:183], v[196:199], v[28:31]
	v_mfma_f32_16x16x32_bf16 v[24:27], v[188:191], v[196:199], v[24:27]
	v_mfma_f32_16x16x32_bf16 v[16:19], v[188:191], v[204:207], v[16:19]
	v_mfma_f32_16x16x32_bf16 v[20:23], v[180:183], v[204:207], v[20:23]
	v_mfma_f32_16x16x32_bf16 v[12:15], v[180:183], v[212:215], v[12:15]
	v_mfma_f32_16x16x32_bf16 v[8:11], v[188:191], v[212:215], v[8:11]
	v_mfma_f32_16x16x32_bf16 v[0:3], v[188:191], v[220:223], v[0:3]
	v_mfma_f32_16x16x32_bf16 v[4:7], v[180:183], v[220:223], v[4:7]
	s_setprio 0
	s_barrier
	s_mov_b32 m0, s33
	s_nop 0
	global_load_lds_dwordx4 v128, s[28:29]
	s_mov_b32 m0, s38
	s_nop 0
	global_load_lds_dwordx4 v130, s[28:29]
	ds_read_b128 v[160:163], v150
	ds_read_b128 v[164:167], v151
	ds_read_b128 v[168:171], v152
	ds_read_b128 v[172:175], v153
	ds_read_b128 v[176:179], v154
	ds_read_b128 v[180:183], v155
	ds_read_b128 v[184:187], v156
	ds_read_b128 v[188:191], v157
	s_add_u32 s28, s28, 0x100000
	s_addc_u32 s29, s29, 0
	s_mov_b32 m0, s39
	ds_read_b128 v[192:195], v158 offset:32768
	ds_read_b128 v[196:199], v158 offset:33792
	ds_read_b128 v[200:203], v158 offset:34816
	ds_read_b128 v[204:207], v158 offset:35840
	ds_read_b128 v[208:211], v158 offset:36864
	ds_read_b128 v[212:215], v158 offset:37888
	ds_read_b128 v[216:219], v158 offset:38912
	ds_read_b128 v[220:223], v158 offset:39936
	global_load_lds_dwordx4 v128, s[28:29]
	s_mov_b32 m0, s40
	s_nop 0
	global_load_lds_dwordx4 v130, s[28:29]
	s_waitcnt vmcnt(8)
	s_waitcnt lgkmcnt(0)
	s_barrier
	s_setprio 1
	s_waitcnt lgkmcnt(0)
	v_mfma_f32_16x16x32_bf16 v[124:127], v[160:163], v[192:195], v[124:127]
	v_mfma_f32_16x16x32_bf16 v[120:123], v[168:171], v[192:195], v[120:123]
	v_mfma_f32_16x16x32_bf16 v[112:115], v[168:171], v[200:203], v[112:115]
	v_mfma_f32_16x16x32_bf16 v[116:119], v[160:163], v[200:203], v[116:119]
	v_mfma_f32_16x16x32_bf16 v[108:111], v[160:163], v[208:211], v[108:111]
	v_mfma_f32_16x16x32_bf16 v[104:107], v[168:171], v[208:211], v[104:107]
	v_mfma_f32_16x16x32_bf16 v[96:99], v[168:171], v[216:219], v[96:99]
	v_mfma_f32_16x16x32_bf16 v[100:103], v[160:163], v[216:219], v[100:103]
	v_mfma_f32_16x16x32_bf16 v[124:127], v[164:167], v[196:199], v[124:127]
	v_mfma_f32_16x16x32_bf16 v[120:123], v[172:175], v[196:199], v[120:123]
	v_mfma_f32_16x16x32_bf16 v[112:115], v[172:175], v[204:207], v[112:115]
	v_mfma_f32_16x16x32_bf16 v[116:119], v[164:167], v[204:207], v[116:119]
	v_mfma_f32_16x16x32_bf16 v[108:111], v[164:167], v[212:215], v[108:111]
	v_mfma_f32_16x16x32_bf16 v[104:107], v[172:175], v[212:215], v[104:107]
	v_mfma_f32_16x16x32_bf16 v[96:99], v[172:175], v[220:223], v[96:99]
	v_mfma_f32_16x16x32_bf16 v[100:103], v[164:167], v[220:223], v[100:103]
	v_mfma_f32_16x16x32_bf16 v[92:95], v[176:179], v[192:195], v[92:95]
	v_mfma_f32_16x16x32_bf16 v[88:91], v[184:187], v[192:195], v[88:91]
	v_mfma_f32_16x16x32_bf16 v[80:83], v[184:187], v[200:203], v[80:83]
	v_mfma_f32_16x16x32_bf16 v[84:87], v[176:179], v[200:203], v[84:87]
	v_mfma_f32_16x16x32_bf16 v[76:79], v[176:179], v[208:211], v[76:79]
	v_mfma_f32_16x16x32_bf16 v[72:75], v[184:187], v[208:211], v[72:75]
	v_mfma_f32_16x16x32_bf16 v[64:67], v[184:187], v[216:219], v[64:67]
	v_mfma_f32_16x16x32_bf16 v[68:71], v[176:179], v[216:219], v[68:71]
	v_mfma_f32_16x16x32_bf16 v[92:95], v[180:183], v[196:199], v[92:95]
	v_mfma_f32_16x16x32_bf16 v[88:91], v[188:191], v[196:199], v[88:91]
	v_mfma_f32_16x16x32_bf16 v[80:83], v[188:191], v[204:207], v[80:83]
	v_mfma_f32_16x16x32_bf16 v[84:87], v[180:183], v[204:207], v[84:87]
	v_mfma_f32_16x16x32_bf16 v[76:79], v[180:183], v[212:215], v[76:79]
	v_mfma_f32_16x16x32_bf16 v[72:75], v[188:191], v[212:215], v[72:75]
	v_mfma_f32_16x16x32_bf16 v[64:67], v[188:191], v[220:223], v[64:67]
	v_mfma_f32_16x16x32_bf16 v[68:71], v[180:183], v[220:223], v[68:71]
	s_setprio 0
	s_barrier
	s_mov_b32 m0, s42
	v_lshl_add_u64 v[224:225], v[224:225], 0, s[10:11]
	s_add_u32 s26, s26, 0x100080
	ds_read_b128 v[192:195], v158 offset:49152
	ds_read_b128 v[196:199], v158 offset:50176
	ds_read_b128 v[200:203], v158 offset:51200
	ds_read_b128 v[204:207], v158 offset:52224
	ds_read_b128 v[208:211], v158 offset:53248
	ds_read_b128 v[212:215], v158 offset:54272
	ds_read_b128 v[216:219], v158 offset:55296
	ds_read_b128 v[220:223], v158 offset:56320
	global_load_lds_dwordx4 v[224:225], off
	v_lshl_add_u64 v[224:225], v[226:227], 0, s[10:11]
	s_mov_b32 m0, s43
	s_addc_u32 s27, s27, 0
	global_load_lds_dwordx4 v[224:225], off
	s_mov_b32 m0, s46
	s_nop 0
	global_load_lds_dwordx4 v128, s[26:27]
	s_mov_b32 m0, s47
	s_nop 0
	global_load_lds_dwordx4 v130, s[26:27]
	s_waitcnt vmcnt(6)
	s_waitcnt lgkmcnt(0)
	s_barrier
	s_setprio 1
	s_waitcnt lgkmcnt(0)
	v_mfma_f32_16x16x32_bf16 v[60:63], v[160:163], v[192:195], v[60:63]
	v_mfma_f32_16x16x32_bf16 v[56:59], v[168:171], v[192:195], v[56:59]
	v_mfma_f32_16x16x32_bf16 v[48:51], v[168:171], v[200:203], v[48:51]
	v_mfma_f32_16x16x32_bf16 v[52:55], v[160:163], v[200:203], v[52:55]
	v_mfma_f32_16x16x32_bf16 v[44:47], v[160:163], v[208:211], v[44:47]
	v_mfma_f32_16x16x32_bf16 v[40:43], v[168:171], v[208:211], v[40:43]
	v_mfma_f32_16x16x32_bf16 v[32:35], v[168:171], v[216:219], v[32:35]
	v_mfma_f32_16x16x32_bf16 v[36:39], v[160:163], v[216:219], v[36:39]
	v_mfma_f32_16x16x32_bf16 v[60:63], v[164:167], v[196:199], v[60:63]
	v_mfma_f32_16x16x32_bf16 v[56:59], v[172:175], v[196:199], v[56:59]
	v_mfma_f32_16x16x32_bf16 v[48:51], v[172:175], v[204:207], v[48:51]
	v_mfma_f32_16x16x32_bf16 v[52:55], v[164:167], v[204:207], v[52:55]
	v_mfma_f32_16x16x32_bf16 v[44:47], v[164:167], v[212:215], v[44:47]
	v_mfma_f32_16x16x32_bf16 v[40:43], v[172:175], v[212:215], v[40:43]
	v_mfma_f32_16x16x32_bf16 v[32:35], v[172:175], v[220:223], v[32:35]
	v_mfma_f32_16x16x32_bf16 v[36:39], v[164:167], v[220:223], v[36:39]
	v_mfma_f32_16x16x32_bf16 v[28:31], v[176:179], v[192:195], v[28:31]
	v_mfma_f32_16x16x32_bf16 v[24:27], v[184:187], v[192:195], v[24:27]
	v_mfma_f32_16x16x32_bf16 v[16:19], v[184:187], v[200:203], v[16:19]
	v_mfma_f32_16x16x32_bf16 v[20:23], v[176:179], v[200:203], v[20:23]
	v_mfma_f32_16x16x32_bf16 v[12:15], v[176:179], v[208:211], v[12:15]
	v_mfma_f32_16x16x32_bf16 v[8:11], v[184:187], v[208:211], v[8:11]
	v_mfma_f32_16x16x32_bf16 v[0:3], v[184:187], v[216:219], v[0:3]
	v_mfma_f32_16x16x32_bf16 v[4:7], v[176:179], v[216:219], v[4:7]
	v_mfma_f32_16x16x32_bf16 v[28:31], v[180:183], v[196:199], v[28:31]
	v_mfma_f32_16x16x32_bf16 v[24:27], v[188:191], v[196:199], v[24:27]
	v_mfma_f32_16x16x32_bf16 v[16:19], v[188:191], v[204:207], v[16:19]
	v_mfma_f32_16x16x32_bf16 v[20:23], v[180:183], v[204:207], v[20:23]
	v_mfma_f32_16x16x32_bf16 v[12:15], v[180:183], v[212:215], v[12:15]
	v_mfma_f32_16x16x32_bf16 v[8:11], v[188:191], v[212:215], v[8:11]
	v_mfma_f32_16x16x32_bf16 v[0:3], v[188:191], v[220:223], v[0:3]
	v_mfma_f32_16x16x32_bf16 v[4:7], v[180:183], v[220:223], v[4:7]
	s_setprio 0
	s_barrier
	s_add_i32 s54, s54, 2
	s_add_u32 s24, s24, 0x100
	s_addc_u32 s25, s25, 0
	s_add_u32 s52, s52, 0x100
	s_addc_u32 s53, s53, 0
	s_cmp_gt_u32 s54, 61
	s_cbranch_scc0 .LBB0_687
	s_and_b64 vcc, exec, s[12:13]
	s_cbranch_vccz .LBB0_690
	s_barrier

.LBB0_1358:
	s_add_u32 s30, s26, 0x1000
	s_addc_u32 s31, s27, 0
	s_mov_b32 m0, s49
	s_nop 0
	global_load_lds_dwordx4 v160, s[30:31]
	s_mov_b32 m0, s50
	s_nop 0
	global_load_lds_dwordx4 v164, s[30:31]
	ds_read_b128 v[16:19], v207
	ds_read_b128 v[20:23], v208
	ds_read_b128 v[24:27], v209
	ds_read_b128 v[28:31], v210
	ds_read_b128 v[0:3], v211
	ds_read_b128 v[4:7], v212
	ds_read_b128 v[8:11], v213
	ds_read_b128 v[12:15], v214
	s_add_u32 s28, s26, 0x10000
	s_addc_u32 s29, s27, 0
	s_cmpk_eq_i32 s59, 0x7c
	s_cselect_b32 s36, s55, s28
	s_cselect_b32 s37, s19, s29
	s_cselect_b32 s34, s56, s57
	s_cselect_b32 s35, s17, s58
	s_add_i32 m0, s25, 0xc000
	ds_read_b128 v[176:179], v224
	ds_read_b128 v[180:183], v224 offset:1024
	ds_read_b128 v[184:187], v224 offset:2048
	ds_read_b128 v[188:191], v224 offset:3072
	ds_read_b128 v[192:195], v224 offset:4096
	ds_read_b128 v[196:199], v224 offset:5120
	ds_read_b128 v[226:229], v224 offset:6144
	ds_read_b128 v[230:233], v224 offset:7168
	global_load_lds_dwordx4 v168, s[26:27]
	s_add_i32 m0, s25, 0xe000
	s_nop 0
	global_load_lds_dwordx4 v170, s[26:27]
	s_waitcnt vmcnt(8)
	s_waitcnt lgkmcnt(0)
	s_barrier
	s_setprio 1
	s_waitcnt lgkmcnt(0)
	v_mfma_f32_16x16x128_f8f6f4 v[156:159], v[16:23], v[176:183], v[156:159]
	v_mfma_f32_16x16x128_f8f6f4 v[152:155], v[24:31], v[176:183], v[152:155]
	v_mfma_f32_16x16x128_f8f6f4 v[136:139], v[24:31], v[184:191], v[136:139]
	v_mfma_f32_16x16x128_f8f6f4 v[144:147], v[16:23], v[184:191], v[144:147]
	v_mfma_f32_16x16x128_f8f6f4 v[124:127], v[16:23], v[192:199], v[124:127]
	v_mfma_f32_16x16x128_f8f6f4 v[120:123], v[24:31], v[192:199], v[120:123]
	v_mfma_f32_16x16x128_f8f6f4 v[104:107], v[24:31], v[226:233], v[104:107]
	v_mfma_f32_16x16x128_f8f6f4 v[112:115], v[16:23], v[226:233], v[112:115]
	v_mfma_f32_16x16x128_f8f6f4 v[100:103], v[0:7], v[226:233], v[100:103]
	v_mfma_f32_16x16x128_f8f6f4 v[96:99], v[8:15], v[226:233], v[96:99]
	v_mfma_f32_16x16x128_f8f6f4 v[108:111], v[8:15], v[192:199], v[108:111]
	v_mfma_f32_16x16x128_f8f6f4 v[116:119], v[0:7], v[192:199], v[116:119]
	v_mfma_f32_16x16x128_f8f6f4 v[132:135], v[0:7], v[184:191], v[132:135]
	v_mfma_f32_16x16x128_f8f6f4 v[128:131], v[8:15], v[184:191], v[128:131]
	v_mfma_f32_16x16x128_f8f6f4 v[140:143], v[8:15], v[176:183], v[140:143]
	v_mfma_f32_16x16x128_f8f6f4 v[148:151], v[0:7], v[176:183], v[148:151]
	s_setprio 0
	s_barrier
	s_mov_b32 m0, s33
	v_lshl_add_u64 v[176:177], s[34:35], 0, v[162:163]
	s_add_u32 s26, s34, 0x200000
	ds_read_b128 v[180:183], v224 offset:16384
	ds_read_b128 v[184:187], v224 offset:17408
	ds_read_b128 v[188:191], v224 offset:18432
	ds_read_b128 v[192:195], v224 offset:19456
	ds_read_b128 v[196:199], v224 offset:20480
	ds_read_b128 v[200:203], v224 offset:21504
	ds_read_b128 v[226:229], v224 offset:22528
	ds_read_b128 v[230:233], v224 offset:23552
	global_load_lds_dwordx4 v[176:177], off
	v_lshl_add_u64 v[178:179], s[34:35], 0, v[166:167]
	s_mov_b32 m0, s38
	s_addc_u32 s27, s35, 0
	global_load_lds_dwordx4 v[178:179], off
	s_mov_b32 m0, s39
	s_nop 0
	global_load_lds_dwordx4 v162, s[26:27]
	s_mov_b32 m0, s40
	s_nop 0
	global_load_lds_dwordx4 v166, s[26:27]
	s_waitcnt vmcnt(6)
	s_waitcnt lgkmcnt(0)
	s_barrier
	s_setprio 1
	s_waitcnt lgkmcnt(0)
	v_mfma_f32_16x16x128_f8f6f4 v[92:95], v[16:23], v[180:187], v[92:95]
	v_mfma_f32_16x16x128_f8f6f4 v[88:91], v[24:31], v[180:187], v[88:91]
	v_mfma_f32_16x16x128_f8f6f4 v[72:75], v[24:31], v[188:195], v[72:75]
	v_mfma_f32_16x16x128_f8f6f4 v[80:83], v[16:23], v[188:195], v[80:83]
	v_mfma_f32_16x16x128_f8f6f4 v[64:67], v[16:23], v[196:203], v[64:67]
	v_mfma_f32_16x16x128_f8f6f4 v[56:59], v[24:31], v[196:203], v[56:59]
	v_mfma_f32_16x16x128_f8f6f4 v[40:43], v[24:31], v[226:233], v[40:43]
	v_mfma_f32_16x16x128_f8f6f4 v[48:51], v[16:23], v[226:233], v[48:51]
	v_mfma_f32_16x16x128_f8f6f4 v[36:39], v[0:7], v[226:233], v[36:39]
	v_mfma_f32_16x16x128_f8f6f4 v[32:35], v[8:15], v[226:233], v[32:35]
	v_mfma_f32_16x16x128_f8f6f4 v[44:47], v[8:15], v[196:203], v[44:47]
	v_mfma_f32_16x16x128_f8f6f4 v[52:55], v[0:7], v[196:203], v[52:55]
	v_mfma_f32_16x16x128_f8f6f4 v[68:71], v[0:7], v[188:195], v[68:71]
	v_mfma_f32_16x16x128_f8f6f4 v[60:63], v[8:15], v[188:195], v[60:63]
	v_mfma_f32_16x16x128_f8f6f4 v[76:79], v[8:15], v[180:187], v[76:79]
	v_mfma_f32_16x16x128_f8f6f4 v[84:87], v[0:7], v[180:187], v[84:87]
	s_setprio 0
	s_barrier
	s_mov_b32 m0, s25
	s_nop 0
	global_load_lds_dwordx4 v160, s[36:37]
	s_mov_b32 m0, s41
	s_nop 0
	global_load_lds_dwordx4 v164, s[36:37]
	ds_read_b128 v[0:3], v215
	ds_read_b128 v[4:7], v216
	ds_read_b128 v[8:11], v217
	ds_read_b128 v[12:15], v218
	ds_read_b128 v[16:19], v219
	ds_read_b128 v[20:23], v220
	ds_read_b128 v[24:27], v221
	ds_read_b128 v[28:31], v222
	s_add_u32 s26, s36, 0x8000
	s_addc_u32 s27, s37, 0
	s_mov_b32 m0, s42
	ds_read_b128 v[180:183], v224 offset:32768
	ds_read_b128 v[184:187], v224 offset:33792
	ds_read_b128 v[188:191], v224 offset:34816
	ds_read_b128 v[192:195], v224 offset:35840
	ds_read_b128 v[196:199], v224 offset:36864
	ds_read_b128 v[200:203], v224 offset:37888
	ds_read_b128 v[226:229], v224 offset:38912
	ds_read_b128 v[230:233], v224 offset:39936
	global_load_lds_dwordx4 v160, s[26:27]
	s_mov_b32 m0, s43
	s_nop 0
	global_load_lds_dwordx4 v164, s[26:27]
	s_waitcnt vmcnt(8)
	s_waitcnt lgkmcnt(0)
	s_barrier
	s_setprio 1
	s_waitcnt lgkmcnt(0)
	v_mfma_f32_16x16x128_f8f6f4 v[156:159], v[0:7], v[180:187], v[156:159]
	v_mfma_f32_16x16x128_f8f6f4 v[152:155], v[8:15], v[180:187], v[152:155]
	v_mfma_f32_16x16x128_f8f6f4 v[136:139], v[8:15], v[188:195], v[136:139]
	v_mfma_f32_16x16x128_f8f6f4 v[144:147], v[0:7], v[188:195], v[144:147]
	v_mfma_f32_16x16x128_f8f6f4 v[124:127], v[0:7], v[196:203], v[124:127]
	v_mfma_f32_16x16x128_f8f6f4 v[120:123], v[8:15], v[196:203], v[120:123]
	v_mfma_f32_16x16x128_f8f6f4 v[104:107], v[8:15], v[226:233], v[104:107]
	v_mfma_f32_16x16x128_f8f6f4 v[112:115], v[0:7], v[226:233], v[112:115]
	v_mfma_f32_16x16x128_f8f6f4 v[100:103], v[16:23], v[226:233], v[100:103]
	v_mfma_f32_16x16x128_f8f6f4 v[96:99], v[24:31], v[226:233], v[96:99]
	v_mfma_f32_16x16x128_f8f6f4 v[108:111], v[24:31], v[196:203], v[108:111]
	v_mfma_f32_16x16x128_f8f6f4 v[116:119], v[16:23], v[196:203], v[116:119]
	v_mfma_f32_16x16x128_f8f6f4 v[132:135], v[16:23], v[188:195], v[132:135]
	v_mfma_f32_16x16x128_f8f6f4 v[128:131], v[24:31], v[188:195], v[128:131]
	v_mfma_f32_16x16x128_f8f6f4 v[140:143], v[24:31], v[180:187], v[140:143]
	v_mfma_f32_16x16x128_f8f6f4 v[148:151], v[16:23], v[180:187], v[148:151]
	s_setprio 0
	s_barrier
	s_mov_b32 m0, s47
	v_lshl_add_u64 v[176:177], v[176:177], 0, s[10:11]
	s_add_u32 s26, s34, 0x200080
	ds_read_b128 v[180:183], v224 offset:49152
	ds_read_b128 v[184:187], v224 offset:50176
	ds_read_b128 v[188:191], v224 offset:51200
	ds_read_b128 v[192:195], v224 offset:52224
	ds_read_b128 v[196:199], v224 offset:53248
	ds_read_b128 v[200:203], v224 offset:54272
	ds_read_b128 v[226:229], v224 offset:55296
	ds_read_b128 v[230:233], v224 offset:56320
	global_load_lds_dwordx4 v[176:177], off
	v_lshl_add_u64 v[176:177], v[178:179], 0, s[10:11]
	s_mov_b32 m0, s48
	s_addc_u32 s27, s35, 0
	global_load_lds_dwordx4 v[176:177], off
	s_mov_b32 m0, s51
	s_nop 0
	global_load_lds_dwordx4 v162, s[26:27]
	s_mov_b32 m0, s52
	s_nop 0
	global_load_lds_dwordx4 v166, s[26:27]
	s_waitcnt vmcnt(6)
	s_waitcnt lgkmcnt(0)
	s_barrier
	s_setprio 1
	s_waitcnt lgkmcnt(0)
	v_mfma_f32_16x16x128_f8f6f4 v[92:95], v[0:7], v[180:187], v[92:95]
	v_mfma_f32_16x16x128_f8f6f4 v[88:91], v[8:15], v[180:187], v[88:91]
	v_mfma_f32_16x16x128_f8f6f4 v[72:75], v[8:15], v[188:195], v[72:75]
	v_mfma_f32_16x16x128_f8f6f4 v[80:83], v[0:7], v[188:195], v[80:83]
	v_mfma_f32_16x16x128_f8f6f4 v[64:67], v[0:7], v[196:203], v[64:67]
	v_mfma_f32_16x16x128_f8f6f4 v[56:59], v[8:15], v[196:203], v[56:59]
	v_mfma_f32_16x16x128_f8f6f4 v[40:43], v[8:15], v[226:233], v[40:43]
	v_mfma_f32_16x16x128_f8f6f4 v[48:51], v[0:7], v[226:233], v[48:51]
	v_mfma_f32_16x16x128_f8f6f4 v[36:39], v[16:23], v[226:233], v[36:39]
	v_mfma_f32_16x16x128_f8f6f4 v[32:35], v[24:31], v[226:233], v[32:35]
	v_mfma_f32_16x16x128_f8f6f4 v[44:47], v[24:31], v[196:203], v[44:47]
	v_mfma_f32_16x16x128_f8f6f4 v[52:55], v[16:23], v[196:203], v[52:55]
	v_mfma_f32_16x16x128_f8f6f4 v[68:71], v[16:23], v[188:195], v[68:71]
	v_mfma_f32_16x16x128_f8f6f4 v[60:63], v[24:31], v[188:195], v[60:63]
	v_mfma_f32_16x16x128_f8f6f4 v[76:79], v[24:31], v[180:187], v[76:79]
	v_mfma_f32_16x16x128_f8f6f4 v[84:87], v[16:23], v[180:187], v[84:87]
	s_setprio 0
	s_barrier
	s_add_i32 s59, s59, 2
	s_add_u32 s57, s57, 0x100
	s_addc_u32 s58, s58, 0
	s_cmpk_gt_u32 s59, 0x7d
	s_mov_b64 s[26:27], s[28:29]
	s_cbranch_scc0 .LBB0_1358
	s_nop 15
	s_nop 15
	s_and_b64 vcc, exec, s[12:13]
	s_cbranch_vccz .LBB0_1361
	s_barrier
